# v8_skipbar
# speedup vs baseline: 1.0402x; 1.0119x over previous
_Z7k_chol2PfS_S_S_PdiPKfS2_S2_S_iS_PDF16_S_:
	s_load_dwordx4 s[60:63], s[0:1], 0x10
	s_load_dword s64, s[0:1], 0x28
	v_readfirstlane_b32 s33, v0
	s_lshr_b32 s86, s33, 6
	v_and_b32_e32 v133, 31, v0
	v_bfe_u32 v132, v0, 5, 1
	s_waitcnt lgkmcnt(0)
	s_sub_i32 s4, 7, s64
	s_sub_i32 s3, 6, s64
	s_mul_i32 s4, s3, s4
	s_lshr_b32 s5, s4, 31
	s_add_i32 s4, s4, s5
	s_lshl_b32 s14, s64, 2
	s_ashr_i32 s22, s4, 1
	s_add_i32 s14, s14, -4
	s_cmp_gt_i32 s64, 1
	s_cselect_b32 s6, s14, 0
	s_add_i32 s7, s22, 1
	s_cmp_lt_i32 s64, 8
	s_cselect_b64 s[8:9], -1, 0
	s_and_b64 s[4:5], s[8:9], exec
	s_cselect_b32 s23, s7, 0
	s_add_i32 s15, s23, s6
	s_cmp_lt_i32 s2, s15
	s_mov_b64 s[4:5], -1
	s_cbranch_scc1 .LBB1_51
	s_load_dwordx2 s[10:11], s[0:1], 0x48
	s_cmp_lg_u32 s64, 8
	s_cbranch_scc0 .LBB1_7
	s_load_dword s16, s[0:1], 0x50
	s_load_dwordx2 s[12:13], s[0:1], 0x40
	s_load_dwordx4 s[4:7], s[0:1], 0x30
	v_mov_b32_e32 v3, 0
	v_lshlrev_b32_e32 v1, 2, v132
	s_waitcnt lgkmcnt(0)
	s_add_i32 s16, s16, s2
	s_sub_i32 s16, s16, s15
	s_lshl_b32 s17, s16, 5
	s_and_b32 s17, s17, 0x3e0
	v_or_b32_e32 v2, s17, v133
	v_lshlrev_b32_e32 v2, 11, v2
	s_and_b32 s15, s16, 0xffffffe0
	v_lshl_add_u64 v[4:5], s[6:7], 0, v[2:3]
	s_lshl_b32 s6, s86, 16
	s_add_i32 s6, s15, s6
	v_lshl_or_b32 v2, s86, 7, v1
	v_lshl_add_u32 v1, v132, 11, s6
	v_or_b32_e32 v1, v1, v133
	v_accvgpr_write_b32 a15, 0
	v_accvgpr_write_b32 a14, 0
	v_accvgpr_write_b32 a13, 0
	v_accvgpr_write_b32 a12, 0
	v_accvgpr_write_b32 a11, 0
	v_accvgpr_write_b32 a10, 0
	v_accvgpr_write_b32 a9, 0
	v_accvgpr_write_b32 a8, 0
	v_accvgpr_write_b32 a7, 0
	v_accvgpr_write_b32 a6, 0
	v_accvgpr_write_b32 a5, 0
	v_accvgpr_write_b32 a4, 0
	v_accvgpr_write_b32 a3, 0
	v_accvgpr_write_b32 a2, 0
	v_accvgpr_write_b32 a1, 0
	v_accvgpr_write_b32 a0, 0
	v_lshlrev_b32_e32 v6, 2, v1
	v_lshl_add_u64 v[8:9], v[2:3], 2, v[4:5]
	v_lshl_add_u64 v[10:11], v[2:3], 2, s[12:13]
	s_mov_b32 s40, s4
	s_mov_b32 s41, s5
	s_add_u32 s42, s4, 0x1000
	s_addc_u32 s43, s5, 0
	global_load_dwordx4 v[12:15], v[8:9], off offset:0
	global_load_dwordx4 v[76:79], v[10:11], off offset:0
	global_load_dword v140, v6, s[40:41]
	global_load_dword v141, v6, s[40:41] offset:2048
	global_load_dword v142, v6, s[42:43]
	global_load_dword v143, v6, s[42:43] offset:2048
	s_add_u32 s40, s40, 0x4000
	s_addc_u32 s41, s41, 0
	s_add_u32 s42, s42, 0x4000
	s_addc_u32 s43, s43, 0
	global_load_dwordx4 v[16:19], v[8:9], off offset:32
	global_load_dwordx4 v[80:83], v[10:11], off offset:32
	global_load_dword v144, v6, s[40:41]
	global_load_dword v145, v6, s[40:41] offset:2048
	global_load_dword v146, v6, s[42:43]
	global_load_dword v147, v6, s[42:43] offset:2048
	s_add_u32 s40, s40, 0x4000
	s_addc_u32 s41, s41, 0
	s_add_u32 s42, s42, 0x4000
	s_addc_u32 s43, s43, 0
	global_load_dwordx4 v[20:23], v[8:9], off offset:64
	global_load_dwordx4 v[84:87], v[10:11], off offset:64
	global_load_dword v148, v6, s[40:41]
	global_load_dword v149, v6, s[40:41] offset:2048
	global_load_dword v150, v6, s[42:43]
	global_load_dword v151, v6, s[42:43] offset:2048
	s_add_u32 s40, s40, 0x4000
	s_addc_u32 s41, s41, 0
	s_add_u32 s42, s42, 0x4000
	s_addc_u32 s43, s43, 0
	global_load_dwordx4 v[24:27], v[8:9], off offset:96
	global_load_dwordx4 v[88:91], v[10:11], off offset:96
	global_load_dword v152, v6, s[40:41]
	global_load_dword v153, v6, s[40:41] offset:2048
	global_load_dword v154, v6, s[42:43]
	global_load_dword v155, v6, s[42:43] offset:2048
	s_add_u32 s40, s40, 0x4000
	s_addc_u32 s41, s41, 0
	s_add_u32 s42, s42, 0x4000
	s_addc_u32 s43, s43, 0
	global_load_dwordx4 v[28:31], v[8:9], off offset:128
	global_load_dwordx4 v[92:95], v[10:11], off offset:128
	global_load_dword v156, v6, s[40:41]
	global_load_dword v157, v6, s[40:41] offset:2048
	global_load_dword v158, v6, s[42:43]
	global_load_dword v159, v6, s[42:43] offset:2048
	s_add_u32 s40, s40, 0x4000
	s_addc_u32 s41, s41, 0
	s_add_u32 s42, s42, 0x4000
	s_addc_u32 s43, s43, 0
	global_load_dwordx4 v[32:35], v[8:9], off offset:160
	global_load_dwordx4 v[96:99], v[10:11], off offset:160
	global_load_dword v160, v6, s[40:41]
	global_load_dword v161, v6, s[40:41] offset:2048
	global_load_dword v162, v6, s[42:43]
	global_load_dword v163, v6, s[42:43] offset:2048
	s_add_u32 s40, s40, 0x4000
	s_addc_u32 s41, s41, 0
	s_add_u32 s42, s42, 0x4000
	s_addc_u32 s43, s43, 0
	global_load_dwordx4 v[36:39], v[8:9], off offset:192
	global_load_dwordx4 v[100:103], v[10:11], off offset:192
	global_load_dword v164, v6, s[40:41]
	global_load_dword v165, v6, s[40:41] offset:2048
	global_load_dword v166, v6, s[42:43]
	global_load_dword v167, v6, s[42:43] offset:2048
	s_add_u32 s40, s40, 0x4000
	s_addc_u32 s41, s41, 0
	s_add_u32 s42, s42, 0x4000
	s_addc_u32 s43, s43, 0
	global_load_dwordx4 v[40:43], v[8:9], off offset:224
	global_load_dwordx4 v[104:107], v[10:11], off offset:224
	global_load_dword v168, v6, s[40:41]
	global_load_dword v169, v6, s[40:41] offset:2048
	global_load_dword v170, v6, s[42:43]
	global_load_dword v171, v6, s[42:43] offset:2048
	s_add_u32 s40, s40, 0x4000
	s_addc_u32 s41, s41, 0
	s_add_u32 s42, s42, 0x4000
	s_addc_u32 s43, s43, 0
	global_load_dwordx4 v[44:47], v[8:9], off offset:256
	global_load_dwordx4 v[108:111], v[10:11], off offset:256
	global_load_dword v172, v6, s[40:41]
	global_load_dword v173, v6, s[40:41] offset:2048
	global_load_dword v174, v6, s[42:43]
	global_load_dword v175, v6, s[42:43] offset:2048
	s_add_u32 s40, s40, 0x4000
	s_addc_u32 s41, s41, 0
	s_add_u32 s42, s42, 0x4000
	s_addc_u32 s43, s43, 0
	global_load_dwordx4 v[48:51], v[8:9], off offset:288
	global_load_dwordx4 v[112:115], v[10:11], off offset:288
	global_load_dword v176, v6, s[40:41]
	global_load_dword v177, v6, s[40:41] offset:2048
	global_load_dword v178, v6, s[42:43]
	global_load_dword v179, v6, s[42:43] offset:2048
	s_add_u32 s40, s40, 0x4000
	s_addc_u32 s41, s41, 0
	s_add_u32 s42, s42, 0x4000
	s_addc_u32 s43, s43, 0
	s_waitcnt vmcnt(54)
	v_mul_f32_e32 v1, v140, v76
	v_mul_f32_e32 v2, v141, v77
	v_mul_f32_e32 v3, v142, v78
	v_mul_f32_e32 v4, v143, v79
	v_mfma_f32_32x32x2_f32 a[0:15], v1, v12, a[0:15]
	global_load_dwordx4 v[52:55], v[8:9], off offset:320
	global_load_dwordx4 v[116:119], v[10:11], off offset:320
	global_load_dword v180, v6, s[40:41]
	global_load_dword v181, v6, s[40:41] offset:2048
	global_load_dword v182, v6, s[42:43]
	global_load_dword v183, v6, s[42:43] offset:2048
	s_add_u32 s40, s40, 0x4000
	s_addc_u32 s41, s41, 0
	s_add_u32 s42, s42, 0x4000
	s_addc_u32 s43, s43, 0
	v_mfma_f32_32x32x2_f32 a[0:15], v2, v13, a[0:15]
	v_mfma_f32_32x32x2_f32 a[0:15], v3, v14, a[0:15]
	v_mfma_f32_32x32x2_f32 a[0:15], v4, v15, a[0:15]
	s_waitcnt vmcnt(54)
	v_mul_f32_e32 v1, v144, v80
	v_mul_f32_e32 v2, v145, v81
	v_mul_f32_e32 v3, v146, v82
	v_mul_f32_e32 v4, v147, v83
	v_mfma_f32_32x32x2_f32 a[0:15], v1, v16, a[0:15]
	global_load_dwordx4 v[56:59], v[8:9], off offset:352
	global_load_dwordx4 v[120:123], v[10:11], off offset:352
	global_load_dword v184, v6, s[40:41]
	global_load_dword v185, v6, s[40:41] offset:2048
	global_load_dword v186, v6, s[42:43]
	global_load_dword v187, v6, s[42:43] offset:2048
	s_add_u32 s40, s40, 0x4000
	s_addc_u32 s41, s41, 0
	s_add_u32 s42, s42, 0x4000
	s_addc_u32 s43, s43, 0
	v_mfma_f32_32x32x2_f32 a[0:15], v2, v17, a[0:15]
	v_mfma_f32_32x32x2_f32 a[0:15], v3, v18, a[0:15]
	v_mfma_f32_32x32x2_f32 a[0:15], v4, v19, a[0:15]
	s_waitcnt vmcnt(54)
	v_mul_f32_e32 v1, v148, v84
	v_mul_f32_e32 v2, v149, v85
	v_mul_f32_e32 v3, v150, v86
	v_mul_f32_e32 v4, v151, v87
	v_mfma_f32_32x32x2_f32 a[0:15], v1, v20, a[0:15]
	global_load_dwordx4 v[60:63], v[8:9], off offset:384
	global_load_dwordx4 v[124:127], v[10:11], off offset:384
	global_load_dword v188, v6, s[40:41]
	global_load_dword v189, v6, s[40:41] offset:2048
	global_load_dword v190, v6, s[42:43]
	global_load_dword v191, v6, s[42:43] offset:2048
	s_add_u32 s40, s40, 0x4000
	s_addc_u32 s41, s41, 0
	s_add_u32 s42, s42, 0x4000
	s_addc_u32 s43, s43, 0
	v_mfma_f32_32x32x2_f32 a[0:15], v2, v21, a[0:15]
	v_mfma_f32_32x32x2_f32 a[0:15], v3, v22, a[0:15]
	v_mfma_f32_32x32x2_f32 a[0:15], v4, v23, a[0:15]
	s_waitcnt vmcnt(54)
	v_mul_f32_e32 v1, v152, v88
	v_mul_f32_e32 v2, v153, v89
	v_mul_f32_e32 v3, v154, v90
	v_mul_f32_e32 v4, v155, v91
	v_mfma_f32_32x32x2_f32 a[0:15], v1, v24, a[0:15]
	global_load_dwordx4 v[64:67], v[8:9], off offset:416
	global_load_dwordx4 v[128:131], v[10:11], off offset:416
	global_load_dword v192, v6, s[40:41]
	global_load_dword v193, v6, s[40:41] offset:2048
	global_load_dword v194, v6, s[42:43]
	global_load_dword v195, v6, s[42:43] offset:2048
	s_add_u32 s40, s40, 0x4000
	s_addc_u32 s41, s41, 0
	s_add_u32 s42, s42, 0x4000
	s_addc_u32 s43, s43, 0
	v_mfma_f32_32x32x2_f32 a[0:15], v2, v25, a[0:15]
	v_mfma_f32_32x32x2_f32 a[0:15], v3, v26, a[0:15]
	v_mfma_f32_32x32x2_f32 a[0:15], v4, v27, a[0:15]
	s_waitcnt vmcnt(54)
	v_mul_f32_e32 v1, v156, v92
	v_mul_f32_e32 v2, v157, v93
	v_mul_f32_e32 v3, v158, v94
	v_mul_f32_e32 v4, v159, v95
	v_mfma_f32_32x32x2_f32 a[0:15], v1, v28, a[0:15]
	global_load_dwordx4 v[68:71], v[8:9], off offset:448
	global_load_dwordx4 v[132:135], v[10:11], off offset:448
	global_load_dword v196, v6, s[40:41]
	global_load_dword v197, v6, s[40:41] offset:2048
	global_load_dword v198, v6, s[42:43]
	global_load_dword v199, v6, s[42:43] offset:2048
	s_add_u32 s40, s40, 0x4000
	s_addc_u32 s41, s41, 0
	s_add_u32 s42, s42, 0x4000
	s_addc_u32 s43, s43, 0
	v_mfma_f32_32x32x2_f32 a[0:15], v2, v29, a[0:15]
	v_mfma_f32_32x32x2_f32 a[0:15], v3, v30, a[0:15]
	v_mfma_f32_32x32x2_f32 a[0:15], v4, v31, a[0:15]
	s_waitcnt vmcnt(54)
	v_mul_f32_e32 v1, v160, v96
	v_mul_f32_e32 v2, v161, v97
	v_mul_f32_e32 v3, v162, v98
	v_mul_f32_e32 v4, v163, v99
	v_mfma_f32_32x32x2_f32 a[0:15], v1, v32, a[0:15]
	global_load_dwordx4 v[72:75], v[8:9], off offset:480
	global_load_dwordx4 v[136:139], v[10:11], off offset:480
	global_load_dword v200, v6, s[40:41]
	global_load_dword v201, v6, s[40:41] offset:2048
	global_load_dword v202, v6, s[42:43]
	global_load_dword v203, v6, s[42:43] offset:2048
	s_add_u32 s40, s40, 0x4000
	s_addc_u32 s41, s41, 0
	s_add_u32 s42, s42, 0x4000
	s_addc_u32 s43, s43, 0
	v_mfma_f32_32x32x2_f32 a[0:15], v2, v33, a[0:15]
	v_mfma_f32_32x32x2_f32 a[0:15], v3, v34, a[0:15]
	v_mfma_f32_32x32x2_f32 a[0:15], v4, v35, a[0:15]
	s_waitcnt vmcnt(54)
	v_mul_f32_e32 v1, v164, v100
	v_mul_f32_e32 v2, v165, v101
	v_mul_f32_e32 v3, v166, v102
	v_mul_f32_e32 v4, v167, v103
	v_mfma_f32_32x32x2_f32 a[0:15], v1, v36, a[0:15]
	v_mfma_f32_32x32x2_f32 a[0:15], v2, v37, a[0:15]
	v_mfma_f32_32x32x2_f32 a[0:15], v3, v38, a[0:15]
	v_mfma_f32_32x32x2_f32 a[0:15], v4, v39, a[0:15]
	s_waitcnt vmcnt(48)
	v_mul_f32_e32 v1, v168, v104
	v_mul_f32_e32 v2, v169, v105
	v_mul_f32_e32 v3, v170, v106
	v_mul_f32_e32 v4, v171, v107
	v_mfma_f32_32x32x2_f32 a[0:15], v1, v40, a[0:15]
	v_mfma_f32_32x32x2_f32 a[0:15], v2, v41, a[0:15]
	v_mfma_f32_32x32x2_f32 a[0:15], v3, v42, a[0:15]
	v_mfma_f32_32x32x2_f32 a[0:15], v4, v43, a[0:15]
	s_waitcnt vmcnt(42)
	v_mul_f32_e32 v1, v172, v108
	v_mul_f32_e32 v2, v173, v109
	v_mul_f32_e32 v3, v174, v110
	v_mul_f32_e32 v4, v175, v111
	v_mfma_f32_32x32x2_f32 a[0:15], v1, v44, a[0:15]
	v_mfma_f32_32x32x2_f32 a[0:15], v2, v45, a[0:15]
	v_mfma_f32_32x32x2_f32 a[0:15], v3, v46, a[0:15]
	v_mfma_f32_32x32x2_f32 a[0:15], v4, v47, a[0:15]
	s_waitcnt vmcnt(36)
	v_mul_f32_e32 v1, v176, v112
	v_mul_f32_e32 v2, v177, v113
	v_mul_f32_e32 v3, v178, v114
	v_mul_f32_e32 v4, v179, v115
	v_mfma_f32_32x32x2_f32 a[0:15], v1, v48, a[0:15]
	v_mfma_f32_32x32x2_f32 a[0:15], v2, v49, a[0:15]
	v_mfma_f32_32x32x2_f32 a[0:15], v3, v50, a[0:15]
	v_mfma_f32_32x32x2_f32 a[0:15], v4, v51, a[0:15]
	s_waitcnt vmcnt(30)
	v_mul_f32_e32 v1, v180, v116
	v_mul_f32_e32 v2, v181, v117
	v_mul_f32_e32 v3, v182, v118
	v_mul_f32_e32 v4, v183, v119
	v_mfma_f32_32x32x2_f32 a[0:15], v1, v52, a[0:15]
	v_mfma_f32_32x32x2_f32 a[0:15], v2, v53, a[0:15]
	v_mfma_f32_32x32x2_f32 a[0:15], v3, v54, a[0:15]
	v_mfma_f32_32x32x2_f32 a[0:15], v4, v55, a[0:15]
	s_waitcnt vmcnt(24)
	v_mul_f32_e32 v1, v184, v120
	v_mul_f32_e32 v2, v185, v121
	v_mul_f32_e32 v3, v186, v122
	v_mul_f32_e32 v4, v187, v123
	v_mfma_f32_32x32x2_f32 a[0:15], v1, v56, a[0:15]
	v_mfma_f32_32x32x2_f32 a[0:15], v2, v57, a[0:15]
	v_mfma_f32_32x32x2_f32 a[0:15], v3, v58, a[0:15]
	v_mfma_f32_32x32x2_f32 a[0:15], v4, v59, a[0:15]
	s_waitcnt vmcnt(18)
	v_mul_f32_e32 v1, v188, v124
	v_mul_f32_e32 v2, v189, v125
	v_mul_f32_e32 v3, v190, v126
	v_mul_f32_e32 v4, v191, v127
	v_mfma_f32_32x32x2_f32 a[0:15], v1, v60, a[0:15]
	v_mfma_f32_32x32x2_f32 a[0:15], v2, v61, a[0:15]
	v_mfma_f32_32x32x2_f32 a[0:15], v3, v62, a[0:15]
	v_mfma_f32_32x32x2_f32 a[0:15], v4, v63, a[0:15]
	s_waitcnt vmcnt(12)
	v_mul_f32_e32 v1, v192, v128
	v_mul_f32_e32 v2, v193, v129
	v_mul_f32_e32 v3, v194, v130
	v_mul_f32_e32 v4, v195, v131
	v_mfma_f32_32x32x2_f32 a[0:15], v1, v64, a[0:15]
	v_mfma_f32_32x32x2_f32 a[0:15], v2, v65, a[0:15]
	v_mfma_f32_32x32x2_f32 a[0:15], v3, v66, a[0:15]
	v_mfma_f32_32x32x2_f32 a[0:15], v4, v67, a[0:15]
	s_waitcnt vmcnt(6)
	v_mul_f32_e32 v1, v196, v132
	v_mul_f32_e32 v2, v197, v133
	v_mul_f32_e32 v3, v198, v134
	v_mul_f32_e32 v4, v199, v135
	v_mfma_f32_32x32x2_f32 a[0:15], v1, v68, a[0:15]
	v_mfma_f32_32x32x2_f32 a[0:15], v2, v69, a[0:15]
	v_mfma_f32_32x32x2_f32 a[0:15], v3, v70, a[0:15]
	v_mfma_f32_32x32x2_f32 a[0:15], v4, v71, a[0:15]
	s_waitcnt vmcnt(0)
	v_mul_f32_e32 v1, v200, v136
	v_mul_f32_e32 v2, v201, v137
	v_mul_f32_e32 v3, v202, v138
	v_mul_f32_e32 v4, v203, v139
	v_mfma_f32_32x32x2_f32 a[0:15], v1, v72, a[0:15]
	v_mfma_f32_32x32x2_f32 a[0:15], v2, v73, a[0:15]
	v_mfma_f32_32x32x2_f32 a[0:15], v3, v74, a[0:15]
	v_mfma_f32_32x32x2_f32 a[0:15], v4, v75, a[0:15]
	v_and_b32_e32 v133, 31, v0
	v_bfe_u32 v132, v0, 5, 1
	s_lshl_b32 s4, s86, 12
	s_addk_i32 s4, 0x4400
	v_lshlrev_b32_e32 v1, 9, v132
	v_lshlrev_b32_e32 v2, 2, v133
	v_or3_b32 v1, s4, v1, v2
	v_mov_b32_e32 v2, 0x4400
	s_and_b32 s4, s16, 31
	v_lshl_or_b32 v4, v0, 2, v2
	v_lshrrev_b32_e32 v2, 5, v0
	s_lshl_b32 s4, s4, 14
	v_lshlrev_b32_e32 v3, 9, v133
	v_or3_b32 v2, v2, s4, v3
	s_nop 4
	ds_write_b32 v1, a0
	ds_write_b32 v1, a1 offset:128
	ds_write_b32 v1, a2 offset:256
	ds_write_b32 v1, a3 offset:384
	ds_write_b32 v1, a4 offset:1024
	ds_write_b32 v1, a5 offset:1152
	ds_write_b32 v1, a6 offset:1280
	ds_write_b32 v1, a7 offset:1408
	ds_write_b32 v1, a8 offset:2048
	ds_write_b32 v1, a9 offset:2176
	ds_write_b32 v1, a10 offset:2304
	ds_write_b32 v1, a11 offset:2432
	ds_write_b32 v1, a12 offset:3072
	ds_write_b32 v1, a13 offset:3200
	ds_write_b32 v1, a14 offset:3328
	ds_write_b32 v1, a15 offset:3456
	v_or_b32_e32 v1, 0xffffff00, v0
	v_add_u32_e32 v2, s15, v2
	s_mov_b64 s[4:5], 0
	s_movk_i32 s6, 0x2ff
	s_waitcnt lgkmcnt(0)
	s_barrier

.LBB1_98:
	s_mov_b32 s59, s56
	s_mov_b64 s[54:55], -1
	s_and_b64 vcc, exec, s[82:83]
	s_waitcnt lgkmcnt(0)
	s_cmp_lg_u32 s59, 0
	s_cbranch_scc1 .Lskip_topbar_1
	s_barrier
.Lskip_topbar_1:
	s_cbranch_vccz .LBB1_104
	s_cmp_le_u32 s59, s73
	s_cbranch_scc1 .LBB1_103
	s_add_i32 s54, s59, -1
	v_accvgpr_write_b32 a3, 0
	v_accvgpr_write_b32 a2, 0
	v_accvgpr_write_b32 a1, 0
	v_accvgpr_write_b32 a0, 0
	v_mov_b32_e32 v66, v146
	v_mov_b32_e32 v67, v162
	s_mov_b32 s55, s69

.LBB1_104:
	s_lshl_b32 s96, s59, 4
	v_or_b32_e32 v164, s96, v131
	s_andn2_b64 vcc, exec, s[54:55]
	v_lshlrev_b32_e32 v163, 2, v164
	s_cbranch_vccnz .LBB1_114
	v_or_b32_e32 v66, s96, v130
	v_mul_lo_u32 v165, v66, s95
	v_add3_u32 v68, v163, v165, s85
	v_mov_b32_e32 v72, v68
	s_nop 0
	ds_read2_b32 v[66:67], v72 offset1:68
	ds_read2_b32 v[68:69], v72 offset0:136 offset1:204
	v_accvgpr_write_b32 a4, v137
	v_accvgpr_write_b32 a5, v138
	v_accvgpr_write_b32 a6, v139
	s_waitcnt lgkmcnt(1)
	v_readlane_b32 s54, v66, 0
	v_accvgpr_write_b32 a7, v140
	v_cmp_lt_i32_e32 vcc, 0, v136
	v_rcp_f32_e64 v73, -s54
	v_writelane_b32 v166, s54, 0
	v_cndmask_b32_e64 v72, 0, v66, s[6:7]
	v_mul_f32_e32 v70, v72, v73
	s_waitcnt lgkmcnt(0)
	s_nop 0
	v_mfma_f32_16x16x4_f32 v[66:69], v70, v66, v[66:69]
	v_mfma_f32_16x16x4_f32 a[4:7], v70, v137, a[4:7]
	s_nop 5
	v_readlane_b32 s54, v67, 1
	v_cndmask_b32_e64 v72, 0, v67, s[8:9]
	s_nop 0
	v_rcp_f32_e64 v73, -s54
	v_writelane_b32 v166, s54, 1
	v_mul_f32_e32 v71, v72, v73
	s_nop 1
	v_mfma_f32_16x16x4_f32 v[66:69], v71, v67, v[66:69]
	v_mfma_f32_16x16x4_f32 a[4:7], v71, a5, a[4:7]
	s_nop 5
	v_readlane_b32 s54, v68, 2
	v_cndmask_b32_e64 v72, 0, v68, s[10:11]
	s_nop 0
	v_rcp_f32_e64 v73, -s54
	v_writelane_b32 v166, s54, 2
	v_mul_f32_e32 v70, v72, v73
	s_nop 1
	v_mfma_f32_16x16x4_f32 v[66:69], v70, v68, v[66:69]
	v_mfma_f32_16x16x4_f32 a[4:7], v70, a6, a[4:7]
	s_nop 5
	v_readlane_b32 s54, v69, 3
	v_cndmask_b32_e64 v72, 0, v69, s[12:13]
	s_nop 0
	v_rcp_f32_e64 v73, -s54
	v_writelane_b32 v166, s54, 3
	v_mul_f32_e32 v71, v72, v73
	s_nop 1
	v_mfma_f32_16x16x4_f32 v[66:69], v71, v69, v[66:69]
	v_mfma_f32_16x16x4_f32 a[4:7], v71, a7, a[4:7]
	s_nop 5
	v_readlane_b32 s54, v66, 20
	v_cndmask_b32_e64 v72, 0, v66, s[14:15]
	s_nop 0
	v_rcp_f32_e64 v73, -s54
	v_writelane_b32 v166, s54, 4
	v_mul_f32_e32 v70, v72, v73
	s_nop 1
	v_mfma_f32_16x16x4_f32 v[66:69], v70, v66, v[66:69]
	v_mfma_f32_16x16x4_f32 a[4:7], v70, a4, a[4:7]
	s_nop 5
	v_readlane_b32 s54, v67, 21
	v_cndmask_b32_e64 v72, 0, v67, s[16:17]
	s_nop 0
	v_rcp_f32_e64 v73, -s54
	v_writelane_b32 v166, s54, 5
	v_mul_f32_e32 v71, v72, v73
	s_nop 1
	v_mfma_f32_16x16x4_f32 v[66:69], v71, v67, v[66:69]
	v_mfma_f32_16x16x4_f32 a[4:7], v71, a5, a[4:7]
	s_nop 5
	v_readlane_b32 s54, v68, 22
	v_cndmask_b32_e64 v72, 0, v68, s[18:19]
	s_nop 0
	v_rcp_f32_e64 v73, -s54
	v_writelane_b32 v166, s54, 6
	v_mul_f32_e32 v70, v72, v73
	s_nop 1
	v_mfma_f32_16x16x4_f32 v[66:69], v70, v68, v[66:69]
	v_mfma_f32_16x16x4_f32 a[4:7], v70, a6, a[4:7]
	s_nop 5
	v_readlane_b32 s54, v69, 23
	v_cndmask_b32_e64 v72, 0, v69, s[20:21]
	s_nop 0
	v_rcp_f32_e64 v73, -s54
	v_writelane_b32 v166, s54, 7
	v_mul_f32_e32 v71, v72, v73
	s_nop 1
	v_mfma_f32_16x16x4_f32 v[66:69], v71, v69, v[66:69]
	v_mfma_f32_16x16x4_f32 a[4:7], v71, a7, a[4:7]
	s_nop 5
	v_readlane_b32 s54, v66, 40
	v_cndmask_b32_e64 v72, 0, v66, s[22:23]
	s_nop 0
	v_rcp_f32_e64 v73, -s54
	v_writelane_b32 v166, s54, 8
	v_mul_f32_e32 v70, v72, v73
	s_nop 1
	v_mfma_f32_16x16x4_f32 v[66:69], v70, v66, v[66:69]
	v_mfma_f32_16x16x4_f32 a[4:7], v70, a4, a[4:7]
	s_nop 5
	v_readlane_b32 s54, v67, 41
	v_cndmask_b32_e64 v72, 0, v67, s[24:25]
	s_nop 0
	v_rcp_f32_e64 v73, -s54
	v_writelane_b32 v166, s54, 9
	v_mul_f32_e32 v71, v72, v73
	s_nop 1
	v_mfma_f32_16x16x4_f32 v[66:69], v71, v67, v[66:69]
	v_mfma_f32_16x16x4_f32 a[4:7], v71, a5, a[4:7]
	s_nop 5
	v_readlane_b32 s54, v68, 42
	v_cndmask_b32_e64 v72, 0, v68, s[26:27]
	s_nop 0
	v_rcp_f32_e64 v73, -s54
	v_writelane_b32 v166, s54, 10
	v_mul_f32_e32 v70, v72, v73
	s_nop 1
	v_mfma_f32_16x16x4_f32 v[66:69], v70, v68, v[66:69]
	v_mfma_f32_16x16x4_f32 a[4:7], v70, a6, a[4:7]
	s_nop 5
	v_readlane_b32 s54, v69, 43
	v_cndmask_b32_e64 v72, 0, v69, s[28:29]
	s_nop 0
	v_rcp_f32_e64 v73, -s54
	v_writelane_b32 v166, s54, 11
	v_mul_f32_e32 v71, v72, v73
	s_nop 1
	v_mfma_f32_16x16x4_f32 v[66:69], v71, v69, v[66:69]
	v_mfma_f32_16x16x4_f32 a[4:7], v71, a7, a[4:7]
	s_nop 5
	v_readlane_b32 s54, v66, 60
	v_cndmask_b32_e64 v72, 0, v66, s[30:31]
	s_nop 0
	v_rcp_f32_e64 v73, -s54
	v_writelane_b32 v166, s54, 12
	v_mul_f32_e32 v70, v72, v73
	s_nop 1
	v_mfma_f32_16x16x4_f32 v[66:69], v70, v66, v[66:69]
	v_mfma_f32_16x16x4_f32 a[4:7], v70, a4, a[4:7]
	s_nop 5
	v_readlane_b32 s54, v67, 61
	v_cndmask_b32_e64 v72, 0, v67, s[34:35]
	s_nop 0
	v_rcp_f32_e64 v73, -s54
	v_writelane_b32 v166, s54, 13
	v_mul_f32_e32 v71, v72, v73
	s_nop 1
	v_mfma_f32_16x16x4_f32 v[66:69], v71, v67, v[66:69]
	v_mfma_f32_16x16x4_f32 a[4:7], v71, a5, a[4:7]
	s_nop 5
	v_readlane_b32 s54, v68, 62
	v_cndmask_b32_e64 v72, 0, v68, s[36:37]
	s_nop 0
	v_rcp_f32_e64 v73, -s54
	v_writelane_b32 v166, s54, 14
	v_mul_f32_e32 v70, v72, v73
	s_nop 1
	v_mfma_f32_16x16x4_f32 v[66:69], v70, v68, v[66:69]
	v_mfma_f32_16x16x4_f32 a[4:7], v70, a6, a[4:7]
	s_nop 5
	v_readlane_b32 s54, v69, 63
	s_nop 2
	v_writelane_b32 v166, s54, 15
	v_accvgpr_read_b32 v73, a7
	v_accvgpr_read_b32 v72, a6
	v_accvgpr_read_b32 v71, a5
	v_accvgpr_read_b32 v70, a4
	s_and_saveexec_b64 s[54:55], s[4:5]
	s_cbranch_execz .LBB1_113
	s_waitcnt lgkmcnt(2)
	v_lshl_add_u32 v167, s96, 2, v134
	ds_write_b32 v167, v166

.LBB1_123:
	s_add_i32 s99, s54, s98
	s_lshr_b32 vcc_lo, s99, 2
	s_add_i32 s99, s99, vcc_lo
	s_and_b32 s99, s99, 3
	s_cmp_lg_u32 s99, s86
	s_cbranch_scc1 .LBB1_122
	ds_read2_b32 v[70:71], v68 offset1:4
	v_add_u32_e32 v72, s97, v67
	v_add_u32_e32 v73, 0x1ed00, v69
	ds_read2_b32 a[0:1], v72 offset1:68
	ds_read2_b32 a[2:3], v72 offset0:136 offset1:204
	ds_read_b32 v73, v73
	s_waitcnt lgkmcnt(3)
	v_xor_b32_e32 v70, 0x80000000, v70
	v_add_u32_e32 v163, 0x1ed10, v69
	v_add_u32_e32 v164, 0x1ed20, v69
	v_add_u32_e32 v165, 0x1ed30, v69
	ds_read_b32 v163, v163
	ds_read_b32 v164, v164
	ds_read_b32 v165, v165
	s_waitcnt lgkmcnt(3)
	v_mfma_f32_16x16x4_f32 a[0:3], v70, v73, a[0:3]
	v_xor_b32_e32 v70, 0x80000000, v71
	s_waitcnt lgkmcnt(2)
	s_nop 0
	v_mfma_f32_16x16x4_f32 a[0:3], v70, v163, a[0:3]
	ds_read2_b32 v[70:71], v68 offset0:8 offset1:12
	s_waitcnt lgkmcnt(0)
	v_xor_b32_e32 v70, 0x80000000, v70
	s_nop 1
	v_mfma_f32_16x16x4_f32 a[0:3], v70, v164, a[0:3]
	v_xor_b32_e32 v70, 0x80000000, v71
	s_nop 1
	v_mfma_f32_16x16x4_f32 a[0:3], v70, v165, a[0:3]
	s_nop 9
	ds_write_b32 v72, a0
	ds_write_b32 v72, a1 offset:272
	ds_write_b32 v72, a2 offset:544
	ds_write_b32 v72, a3 offset:816
	s_branch .LBB1_122

.LBB1_219:
	s_mov_b32 s59, s56
	s_mov_b64 s[52:53], -1
	s_and_b64 vcc, exec, s[82:83]
	s_waitcnt lgkmcnt(0)
	s_cmp_lg_u32 s59, 0
	s_cbranch_scc1 .Lskip_topbar_2
	s_barrier
.Lskip_topbar_2:
	s_cbranch_vccz .LBB1_225
	s_cmp_le_u32 s59, s73
	s_cbranch_scc1 .LBB1_224
	s_add_i32 s52, s59, -1
	v_accvgpr_write_b32 a3, 0
	v_accvgpr_write_b32 a2, 0
	v_accvgpr_write_b32 a1, 0
	v_accvgpr_write_b32 a0, 0
	v_mov_b32_e32 v2, v146
	v_mov_b32_e32 v3, v145
	s_mov_b32 s53, s69

.LBB1_225:
	s_lshl_b32 s97, s59, 4
	v_or_b32_e32 v14, s97, v131
	s_andn2_b64 vcc, exec, s[52:53]
	v_lshlrev_b32_e32 v13, 2, v14
	s_cbranch_vccnz .LBB1_235
	v_or_b32_e32 v2, s97, v130
	v_mul_lo_u32 v15, v2, s57
	v_add3_u32 v4, v13, v15, s95
	v_mov_b32_e32 v8, v4
	s_nop 0
	ds_read2_b32 v[2:3], v8 offset1:68
	ds_read2_b32 v[4:5], v8 offset0:136 offset1:204
	v_accvgpr_write_b32 a4, v137
	v_accvgpr_write_b32 a5, v138
	v_accvgpr_write_b32 a6, v139
	s_waitcnt lgkmcnt(1)
	v_readlane_b32 s52, v2, 0
	v_accvgpr_write_b32 a7, v140
	v_cmp_lt_i32_e32 vcc, 0, v136
	v_rcp_f32_e64 v9, -s52
	v_writelane_b32 v16, s52, 0
	v_cndmask_b32_e64 v8, 0, v2, s[6:7]
	v_mul_f32_e32 v6, v8, v9
	s_waitcnt lgkmcnt(0)
	s_nop 0
	v_mfma_f32_16x16x4_f32 v[2:5], v6, v2, v[2:5]
	v_mfma_f32_16x16x4_f32 a[4:7], v6, v137, a[4:7]
	s_nop 5
	v_readlane_b32 s52, v3, 1
	v_cndmask_b32_e64 v8, 0, v3, s[8:9]
	s_nop 0
	v_rcp_f32_e64 v9, -s52
	v_writelane_b32 v16, s52, 1
	v_mul_f32_e32 v7, v8, v9
	s_nop 1
	v_mfma_f32_16x16x4_f32 v[2:5], v7, v3, v[2:5]
	v_mfma_f32_16x16x4_f32 a[4:7], v7, a5, a[4:7]
	s_nop 5
	v_readlane_b32 s52, v4, 2
	v_cndmask_b32_e64 v8, 0, v4, s[10:11]
	s_nop 0
	v_rcp_f32_e64 v9, -s52
	v_writelane_b32 v16, s52, 2
	v_mul_f32_e32 v6, v8, v9
	s_nop 1
	v_mfma_f32_16x16x4_f32 v[2:5], v6, v4, v[2:5]
	v_mfma_f32_16x16x4_f32 a[4:7], v6, a6, a[4:7]
	s_nop 5
	v_readlane_b32 s52, v5, 3
	v_cndmask_b32_e64 v8, 0, v5, s[12:13]
	s_nop 0
	v_rcp_f32_e64 v9, -s52
	v_writelane_b32 v16, s52, 3
	v_mul_f32_e32 v7, v8, v9
	s_nop 1
	v_mfma_f32_16x16x4_f32 v[2:5], v7, v5, v[2:5]
	v_mfma_f32_16x16x4_f32 a[4:7], v7, a7, a[4:7]
	s_nop 5
	v_readlane_b32 s52, v2, 20
	v_cndmask_b32_e64 v8, 0, v2, s[14:15]
	s_nop 0
	v_rcp_f32_e64 v9, -s52
	v_writelane_b32 v16, s52, 4
	v_mul_f32_e32 v6, v8, v9
	s_nop 1
	v_mfma_f32_16x16x4_f32 v[2:5], v6, v2, v[2:5]
	v_mfma_f32_16x16x4_f32 a[4:7], v6, a4, a[4:7]
	s_nop 5
	v_readlane_b32 s52, v3, 21
	v_cndmask_b32_e64 v8, 0, v3, s[16:17]
	s_nop 0
	v_rcp_f32_e64 v9, -s52
	v_writelane_b32 v16, s52, 5
	v_mul_f32_e32 v7, v8, v9
	s_nop 1
	v_mfma_f32_16x16x4_f32 v[2:5], v7, v3, v[2:5]
	v_mfma_f32_16x16x4_f32 a[4:7], v7, a5, a[4:7]
	s_nop 5
	v_readlane_b32 s52, v4, 22
	v_cndmask_b32_e64 v8, 0, v4, s[18:19]
	s_nop 0
	v_rcp_f32_e64 v9, -s52
	v_writelane_b32 v16, s52, 6
	v_mul_f32_e32 v6, v8, v9
	s_nop 1
	v_mfma_f32_16x16x4_f32 v[2:5], v6, v4, v[2:5]
	v_mfma_f32_16x16x4_f32 a[4:7], v6, a6, a[4:7]
	s_nop 5
	v_readlane_b32 s52, v5, 23
	v_cndmask_b32_e64 v8, 0, v5, s[20:21]
	s_nop 0
	v_rcp_f32_e64 v9, -s52
	v_writelane_b32 v16, s52, 7
	v_mul_f32_e32 v7, v8, v9
	s_nop 1
	v_mfma_f32_16x16x4_f32 v[2:5], v7, v5, v[2:5]
	v_mfma_f32_16x16x4_f32 a[4:7], v7, a7, a[4:7]
	s_nop 5
	v_readlane_b32 s52, v2, 40
	v_cndmask_b32_e64 v8, 0, v2, s[22:23]
	s_nop 0
	v_rcp_f32_e64 v9, -s52
	v_writelane_b32 v16, s52, 8
	v_mul_f32_e32 v6, v8, v9
	s_nop 1
	v_mfma_f32_16x16x4_f32 v[2:5], v6, v2, v[2:5]
	v_mfma_f32_16x16x4_f32 a[4:7], v6, a4, a[4:7]
	s_nop 5
	v_readlane_b32 s52, v3, 41
	v_cndmask_b32_e64 v8, 0, v3, s[24:25]
	s_nop 0
	v_rcp_f32_e64 v9, -s52
	v_writelane_b32 v16, s52, 9
	v_mul_f32_e32 v7, v8, v9
	s_nop 1
	v_mfma_f32_16x16x4_f32 v[2:5], v7, v3, v[2:5]
	v_mfma_f32_16x16x4_f32 a[4:7], v7, a5, a[4:7]
	s_nop 5
	v_readlane_b32 s52, v4, 42
	v_cndmask_b32_e64 v8, 0, v4, s[26:27]
	s_nop 0
	v_rcp_f32_e64 v9, -s52
	v_writelane_b32 v16, s52, 10
	v_mul_f32_e32 v6, v8, v9
	s_nop 1
	v_mfma_f32_16x16x4_f32 v[2:5], v6, v4, v[2:5]
	v_mfma_f32_16x16x4_f32 a[4:7], v6, a6, a[4:7]
	s_nop 5
	v_readlane_b32 s52, v5, 43
	v_cndmask_b32_e64 v8, 0, v5, s[28:29]
	s_nop 0
	v_rcp_f32_e64 v9, -s52
	v_writelane_b32 v16, s52, 11
	v_mul_f32_e32 v7, v8, v9
	s_nop 1
	v_mfma_f32_16x16x4_f32 v[2:5], v7, v5, v[2:5]
	v_mfma_f32_16x16x4_f32 a[4:7], v7, a7, a[4:7]
	s_nop 5
	v_readlane_b32 s52, v2, 60
	v_cndmask_b32_e64 v8, 0, v2, s[30:31]
	s_nop 0
	v_rcp_f32_e64 v9, -s52
	v_writelane_b32 v16, s52, 12
	v_mul_f32_e32 v6, v8, v9
	s_nop 1
	v_mfma_f32_16x16x4_f32 v[2:5], v6, v2, v[2:5]
	v_mfma_f32_16x16x4_f32 a[4:7], v6, a4, a[4:7]
	s_nop 5
	v_readlane_b32 s52, v3, 61
	v_cndmask_b32_e64 v8, 0, v3, s[34:35]
	s_nop 0
	v_rcp_f32_e64 v9, -s52
	v_writelane_b32 v16, s52, 13
	v_mul_f32_e32 v7, v8, v9
	s_nop 1
	v_mfma_f32_16x16x4_f32 v[2:5], v7, v3, v[2:5]
	v_mfma_f32_16x16x4_f32 a[4:7], v7, a5, a[4:7]
	s_nop 5
	v_readlane_b32 s52, v4, 62
	v_cndmask_b32_e64 v8, 0, v4, s[36:37]
	s_nop 0
	v_rcp_f32_e64 v9, -s52
	v_writelane_b32 v16, s52, 14
	v_mul_f32_e32 v6, v8, v9
	s_nop 1
	v_mfma_f32_16x16x4_f32 v[2:5], v6, v4, v[2:5]
	v_mfma_f32_16x16x4_f32 a[4:7], v6, a6, a[4:7]
	s_nop 5
	v_readlane_b32 s52, v5, 63
	s_nop 2
	v_writelane_b32 v16, s52, 15
	v_accvgpr_read_b32 v9, a7
	v_accvgpr_read_b32 v8, a6
	v_accvgpr_read_b32 v7, a5
	v_accvgpr_read_b32 v6, a4
	s_and_saveexec_b64 s[52:53], s[4:5]
	s_cbranch_execz .LBB1_234
	s_waitcnt lgkmcnt(2)
	v_lshl_add_u32 v17, s97, 2, v134
	ds_write_b32 v17, v16

.LBB1_244:
	s_add_i32 s99, s52, s98
	s_lshr_b32 vcc_lo, s99, 2
	s_add_i32 s99, s99, vcc_lo
	s_and_b32 s99, s99, 3
	s_cmp_lg_u32 s99, s86
	s_cbranch_scc1 .LBB1_243
	ds_read2_b32 v[6:7], v4 offset1:4
	v_add_u32_e32 v8, s97, v3
	v_add_u32_e32 v9, 0x1a900, v5
	ds_read2_b32 a[0:1], v8 offset1:68
	ds_read2_b32 a[2:3], v8 offset0:136 offset1:204
	ds_read_b32 v9, v9
	s_waitcnt lgkmcnt(3)
	v_xor_b32_e32 v6, 0x80000000, v6
	v_add_u32_e32 v13, 0x1a910, v5
	v_add_u32_e32 v14, 0x1a920, v5
	v_add_u32_e32 v15, 0x1a930, v5
	ds_read_b32 v13, v13
	ds_read_b32 v14, v14
	ds_read_b32 v15, v15
	s_waitcnt lgkmcnt(3)
	v_mfma_f32_16x16x4_f32 a[0:3], v6, v9, a[0:3]
	v_xor_b32_e32 v6, 0x80000000, v7
	s_waitcnt lgkmcnt(2)
	s_nop 0
	v_mfma_f32_16x16x4_f32 a[0:3], v6, v13, a[0:3]
	ds_read2_b32 v[6:7], v4 offset0:8 offset1:12
	s_waitcnt lgkmcnt(0)
	v_xor_b32_e32 v6, 0x80000000, v6
	s_nop 1
	v_mfma_f32_16x16x4_f32 a[0:3], v6, v14, a[0:3]
	v_xor_b32_e32 v6, 0x80000000, v7
	s_nop 1
	v_mfma_f32_16x16x4_f32 a[0:3], v6, v15, a[0:3]
	s_nop 9
	ds_write_b32 v8, a0
	ds_write_b32 v8, a1 offset:272
	ds_write_b32 v8, a2 offset:544
	ds_write_b32 v8, a3 offset:816
	s_branch .LBB1_243

.LBB1_289:
	s_mov_b32 s79, s52
	s_mov_b64 s[52:53], -1
	s_and_b64 vcc, exec, s[56:57]
	s_waitcnt lgkmcnt(0)
	s_cmp_lg_u32 s79, 0
	s_cbranch_scc1 .Lskip_topbar_3
	s_barrier
.Lskip_topbar_3:
	s_cbranch_vccz .LBB1_295
	s_cmp_le_u32 s79, s71
	s_cbranch_scc1 .LBB1_294
	s_add_i32 s52, s79, -1
	v_accvgpr_write_b32 a3, 0
	v_accvgpr_write_b32 a2, 0
	v_accvgpr_write_b32 a1, 0
	v_accvgpr_write_b32 a0, 0
	v_mov_b32_e32 v2, v31
	v_mov_b32_e32 v3, v40
	s_mov_b32 s53, s70

.LBB1_295:
	s_lshl_b32 s80, s79, 4
	v_or_b32_e32 v42, s80, v19
	s_andn2_b64 vcc, exec, s[52:53]
	v_lshlrev_b32_e32 v41, 2, v42
	s_cbranch_vccnz .LBB1_305
	v_or_b32_e32 v2, s80, v18
	v_mul_lo_u32 v44, v2, s78
	v_add3_u32 v4, v41, v44, s69
	v_mov_b32_e32 v8, v4
	s_nop 0
	ds_read2_b32 v[2:3], v8 offset1:68
	ds_read2_b32 v[4:5], v8 offset0:136 offset1:204
	v_accvgpr_write_b32 a4, v22
	v_accvgpr_write_b32 a5, v23
	v_accvgpr_write_b32 a6, v24
	s_waitcnt lgkmcnt(1)
	v_readlane_b32 s52, v2, 0
	v_accvgpr_write_b32 a7, v25
	v_cmp_lt_i32_e32 vcc, 0, v21
	v_rcp_f32_e64 v9, -s52
	v_writelane_b32 v53, s52, 0
	v_cndmask_b32_e64 v8, 0, v2, s[4:5]
	v_mul_f32_e32 v6, v8, v9
	s_waitcnt lgkmcnt(0)
	s_nop 0
	v_mfma_f32_16x16x4_f32 v[2:5], v6, v2, v[2:5]
	v_mfma_f32_16x16x4_f32 a[4:7], v6, v22, a[4:7]
	s_nop 5
	v_readlane_b32 s52, v3, 1
	v_cndmask_b32_e64 v8, 0, v3, s[6:7]
	s_nop 0
	v_rcp_f32_e64 v9, -s52
	v_writelane_b32 v53, s52, 1
	v_mul_f32_e32 v7, v8, v9
	s_nop 1
	v_mfma_f32_16x16x4_f32 v[2:5], v7, v3, v[2:5]
	v_mfma_f32_16x16x4_f32 a[4:7], v7, a5, a[4:7]
	s_nop 5
	v_readlane_b32 s52, v4, 2
	v_cndmask_b32_e64 v8, 0, v4, s[8:9]
	s_nop 0
	v_rcp_f32_e64 v9, -s52
	v_writelane_b32 v53, s52, 2
	v_mul_f32_e32 v6, v8, v9
	s_nop 1
	v_mfma_f32_16x16x4_f32 v[2:5], v6, v4, v[2:5]
	v_mfma_f32_16x16x4_f32 a[4:7], v6, a6, a[4:7]
	s_nop 5
	v_readlane_b32 s52, v5, 3
	v_cndmask_b32_e64 v8, 0, v5, s[10:11]
	s_nop 0
	v_rcp_f32_e64 v9, -s52
	v_writelane_b32 v53, s52, 3
	v_mul_f32_e32 v7, v8, v9
	s_nop 1
	v_mfma_f32_16x16x4_f32 v[2:5], v7, v5, v[2:5]
	v_mfma_f32_16x16x4_f32 a[4:7], v7, a7, a[4:7]
	s_nop 5
	v_readlane_b32 s52, v2, 20
	v_cndmask_b32_e64 v8, 0, v2, s[12:13]
	s_nop 0
	v_rcp_f32_e64 v9, -s52
	v_writelane_b32 v53, s52, 4
	v_mul_f32_e32 v6, v8, v9
	s_nop 1
	v_mfma_f32_16x16x4_f32 v[2:5], v6, v2, v[2:5]
	v_mfma_f32_16x16x4_f32 a[4:7], v6, a4, a[4:7]
	s_nop 5
	v_readlane_b32 s52, v3, 21
	v_cndmask_b32_e64 v8, 0, v3, s[14:15]
	s_nop 0
	v_rcp_f32_e64 v9, -s52
	v_writelane_b32 v53, s52, 5
	v_mul_f32_e32 v7, v8, v9
	s_nop 1
	v_mfma_f32_16x16x4_f32 v[2:5], v7, v3, v[2:5]
	v_mfma_f32_16x16x4_f32 a[4:7], v7, a5, a[4:7]
	s_nop 5
	v_readlane_b32 s52, v4, 22
	v_cndmask_b32_e64 v8, 0, v4, s[16:17]
	s_nop 0
	v_rcp_f32_e64 v9, -s52
	v_writelane_b32 v53, s52, 6
	v_mul_f32_e32 v6, v8, v9
	s_nop 1
	v_mfma_f32_16x16x4_f32 v[2:5], v6, v4, v[2:5]
	v_mfma_f32_16x16x4_f32 a[4:7], v6, a6, a[4:7]
	s_nop 5
	v_readlane_b32 s52, v5, 23
	v_cndmask_b32_e64 v8, 0, v5, s[18:19]
	s_nop 0
	v_rcp_f32_e64 v9, -s52
	v_writelane_b32 v53, s52, 7
	v_mul_f32_e32 v7, v8, v9
	s_nop 1
	v_mfma_f32_16x16x4_f32 v[2:5], v7, v5, v[2:5]
	v_mfma_f32_16x16x4_f32 a[4:7], v7, a7, a[4:7]
	s_nop 5
	v_readlane_b32 s52, v2, 40
	v_cndmask_b32_e64 v8, 0, v2, s[20:21]
	s_nop 0
	v_rcp_f32_e64 v9, -s52
	v_writelane_b32 v53, s52, 8
	v_mul_f32_e32 v6, v8, v9
	s_nop 1
	v_mfma_f32_16x16x4_f32 v[2:5], v6, v2, v[2:5]
	v_mfma_f32_16x16x4_f32 a[4:7], v6, a4, a[4:7]
	s_nop 5
	v_readlane_b32 s52, v3, 41
	v_cndmask_b32_e64 v8, 0, v3, s[22:23]
	s_nop 0
	v_rcp_f32_e64 v9, -s52
	v_writelane_b32 v53, s52, 9
	v_mul_f32_e32 v7, v8, v9
	s_nop 1
	v_mfma_f32_16x16x4_f32 v[2:5], v7, v3, v[2:5]
	v_mfma_f32_16x16x4_f32 a[4:7], v7, a5, a[4:7]
	s_nop 5
	v_readlane_b32 s52, v4, 42
	v_cndmask_b32_e64 v8, 0, v4, s[24:25]
	s_nop 0
	v_rcp_f32_e64 v9, -s52
	v_writelane_b32 v53, s52, 10
	v_mul_f32_e32 v6, v8, v9
	s_nop 1
	v_mfma_f32_16x16x4_f32 v[2:5], v6, v4, v[2:5]
	v_mfma_f32_16x16x4_f32 a[4:7], v6, a6, a[4:7]
	s_nop 5
	v_readlane_b32 s52, v5, 43
	v_cndmask_b32_e64 v8, 0, v5, s[26:27]
	s_nop 0
	v_rcp_f32_e64 v9, -s52
	v_writelane_b32 v53, s52, 11
	v_mul_f32_e32 v7, v8, v9
	s_nop 1
	v_mfma_f32_16x16x4_f32 v[2:5], v7, v5, v[2:5]
	v_mfma_f32_16x16x4_f32 a[4:7], v7, a7, a[4:7]
	s_nop 5
	v_readlane_b32 s52, v2, 60
	v_cndmask_b32_e64 v8, 0, v2, s[28:29]
	s_nop 0
	v_rcp_f32_e64 v9, -s52
	v_writelane_b32 v53, s52, 12
	v_mul_f32_e32 v6, v8, v9
	s_nop 1
	v_mfma_f32_16x16x4_f32 v[2:5], v6, v2, v[2:5]
	v_mfma_f32_16x16x4_f32 a[4:7], v6, a4, a[4:7]
	s_nop 5
	v_readlane_b32 s52, v3, 61
	v_cndmask_b32_e64 v8, 0, v3, s[30:31]
	s_nop 0
	v_rcp_f32_e64 v9, -s52
	v_writelane_b32 v53, s52, 13
	v_mul_f32_e32 v7, v8, v9
	s_nop 1
	v_mfma_f32_16x16x4_f32 v[2:5], v7, v3, v[2:5]
	v_mfma_f32_16x16x4_f32 a[4:7], v7, a5, a[4:7]
	s_nop 5
	v_readlane_b32 s52, v4, 62
	v_cndmask_b32_e64 v8, 0, v4, s[34:35]
	s_nop 0
	v_rcp_f32_e64 v9, -s52
	v_writelane_b32 v53, s52, 14
	v_mul_f32_e32 v6, v8, v9
	s_nop 1
	v_mfma_f32_16x16x4_f32 v[2:5], v6, v4, v[2:5]
	v_mfma_f32_16x16x4_f32 a[4:7], v6, a6, a[4:7]
	s_nop 5
	v_readlane_b32 s52, v5, 63
	s_nop 2
	v_writelane_b32 v53, s52, 15
	v_accvgpr_read_b32 v9, a7
	v_accvgpr_read_b32 v8, a6
	v_accvgpr_read_b32 v7, a5
	v_accvgpr_read_b32 v6, a4
	s_and_saveexec_b64 s[52:53], s[2:3]
	s_cbranch_execz .LBB1_304
	s_waitcnt lgkmcnt(2)
	v_lshl_add_u32 v54, s80, 2, v11
	ds_write_b32 v54, v53

.LBB1_314:
	s_add_i32 s83, s53, s82
	s_lshr_b32 vcc_lo, s83, 2
	s_add_i32 s83, s83, vcc_lo
	s_and_b32 s83, s83, 3
	s_cmp_lg_u32 s83, s86
	s_cbranch_scc1 .LBB1_313
	ds_read2_b32 v[6:7], v4 offset1:4
	v_add_u32_e32 v8, s81, v3
	v_add_u32_e32 v9, 0x1ed00, v5
	ds_read2_b32 a[0:1], v8 offset1:68
	ds_read2_b32 a[2:3], v8 offset0:136 offset1:204
	ds_read_b32 v9, v9
	s_waitcnt lgkmcnt(3)
	v_xor_b32_e32 v6, 0x80000000, v6
	v_add_u32_e32 v41, 0x1ed10, v5
	v_add_u32_e32 v42, 0x1ed20, v5
	v_add_u32_e32 v44, 0x1ed30, v5
	ds_read_b32 v41, v41
	ds_read_b32 v42, v42
	ds_read_b32 v44, v44
	s_waitcnt lgkmcnt(3)
	v_mfma_f32_16x16x4_f32 a[0:3], v6, v9, a[0:3]
	v_xor_b32_e32 v6, 0x80000000, v7
	s_waitcnt lgkmcnt(2)
	s_nop 0
	v_mfma_f32_16x16x4_f32 a[0:3], v6, v41, a[0:3]
	ds_read2_b32 v[6:7], v4 offset0:8 offset1:12
	s_waitcnt lgkmcnt(0)
	v_xor_b32_e32 v6, 0x80000000, v6
	s_nop 1
	v_mfma_f32_16x16x4_f32 a[0:3], v6, v42, a[0:3]
	v_xor_b32_e32 v6, 0x80000000, v7
	s_nop 1
	v_mfma_f32_16x16x4_f32 a[0:3], v6, v44, a[0:3]
	s_nop 9
	ds_write_b32 v8, a0
	ds_write_b32 v8, a1 offset:272
	ds_write_b32 v8, a2 offset:544
	ds_write_b32 v8, a3 offset:816
	s_branch .LBB1_313

.LBB1_330:
	s_mov_b32 s74, s52
	s_mov_b64 s[52:53], -1
	s_and_b64 vcc, exec, s[56:57]
	s_waitcnt lgkmcnt(0)
	s_cmp_lg_u32 s74, 0
	s_cbranch_scc1 .Lskip_topbar_4
	s_barrier
.Lskip_topbar_4:
	s_cbranch_vccz .LBB1_336
	s_cmp_le_u32 s74, s71
	s_cbranch_scc1 .LBB1_335
	s_add_i32 s52, s74, -1
	v_accvgpr_write_b32 a3, 0
	v_accvgpr_write_b32 a2, 0
	v_accvgpr_write_b32 a1, 0
	v_accvgpr_write_b32 a0, 0
	v_mov_b32_e32 v0, v31
	v_mov_b32_e32 v1, v30
	s_mov_b32 s53, s70

.LBB1_336:
	s_lshl_b32 s75, s74, 4
	v_or_b32_e32 v34, s75, v19
	s_andn2_b64 vcc, exec, s[52:53]
	v_lshlrev_b32_e32 v14, 2, v34
	s_cbranch_vccnz .LBB1_346
	v_or_b32_e32 v0, s75, v18
	v_mul_lo_u32 v35, v0, s64
	v_add3_u32 v2, v14, v35, s72
	v_mov_b32_e32 v6, v2
	s_nop 0
	ds_read2_b32 v[0:1], v6 offset1:68
	ds_read2_b32 v[2:3], v6 offset0:136 offset1:204
	v_accvgpr_write_b32 a4, v22
	v_accvgpr_write_b32 a5, v23
	v_accvgpr_write_b32 a6, v24
	s_waitcnt lgkmcnt(1)
	v_readlane_b32 s52, v0, 0
	v_accvgpr_write_b32 a7, v25
	v_cmp_lt_i32_e32 vcc, 0, v21
	v_rcp_f32_e64 v7, -s52
	v_writelane_b32 v36, s52, 0
	v_cndmask_b32_e64 v6, 0, v0, s[4:5]
	v_mul_f32_e32 v4, v6, v7
	s_waitcnt lgkmcnt(0)
	s_nop 0
	v_mfma_f32_16x16x4_f32 v[0:3], v4, v0, v[0:3]
	v_mfma_f32_16x16x4_f32 a[4:7], v4, v22, a[4:7]
	s_nop 5
	v_readlane_b32 s52, v1, 1
	v_cndmask_b32_e64 v6, 0, v1, s[6:7]
	s_nop 0
	v_rcp_f32_e64 v7, -s52
	v_writelane_b32 v36, s52, 1
	v_mul_f32_e32 v5, v6, v7
	s_nop 1
	v_mfma_f32_16x16x4_f32 v[0:3], v5, v1, v[0:3]
	v_mfma_f32_16x16x4_f32 a[4:7], v5, a5, a[4:7]
	s_nop 5
	v_readlane_b32 s52, v2, 2
	v_cndmask_b32_e64 v6, 0, v2, s[8:9]
	s_nop 0
	v_rcp_f32_e64 v7, -s52
	v_writelane_b32 v36, s52, 2
	v_mul_f32_e32 v4, v6, v7
	s_nop 1
	v_mfma_f32_16x16x4_f32 v[0:3], v4, v2, v[0:3]
	v_mfma_f32_16x16x4_f32 a[4:7], v4, a6, a[4:7]
	s_nop 5
	v_readlane_b32 s52, v3, 3
	v_cndmask_b32_e64 v6, 0, v3, s[10:11]
	s_nop 0
	v_rcp_f32_e64 v7, -s52
	v_writelane_b32 v36, s52, 3
	v_mul_f32_e32 v5, v6, v7
	s_nop 1
	v_mfma_f32_16x16x4_f32 v[0:3], v5, v3, v[0:3]
	v_mfma_f32_16x16x4_f32 a[4:7], v5, a7, a[4:7]
	s_nop 5
	v_readlane_b32 s52, v0, 20
	v_cndmask_b32_e64 v6, 0, v0, s[12:13]
	s_nop 0
	v_rcp_f32_e64 v7, -s52
	v_writelane_b32 v36, s52, 4
	v_mul_f32_e32 v4, v6, v7
	s_nop 1
	v_mfma_f32_16x16x4_f32 v[0:3], v4, v0, v[0:3]
	v_mfma_f32_16x16x4_f32 a[4:7], v4, a4, a[4:7]
	s_nop 5
	v_readlane_b32 s52, v1, 21
	v_cndmask_b32_e64 v6, 0, v1, s[14:15]
	s_nop 0
	v_rcp_f32_e64 v7, -s52
	v_writelane_b32 v36, s52, 5
	v_mul_f32_e32 v5, v6, v7
	s_nop 1
	v_mfma_f32_16x16x4_f32 v[0:3], v5, v1, v[0:3]
	v_mfma_f32_16x16x4_f32 a[4:7], v5, a5, a[4:7]
	s_nop 5
	v_readlane_b32 s52, v2, 22
	v_cndmask_b32_e64 v6, 0, v2, s[16:17]
	s_nop 0
	v_rcp_f32_e64 v7, -s52
	v_writelane_b32 v36, s52, 6
	v_mul_f32_e32 v4, v6, v7
	s_nop 1
	v_mfma_f32_16x16x4_f32 v[0:3], v4, v2, v[0:3]
	v_mfma_f32_16x16x4_f32 a[4:7], v4, a6, a[4:7]
	s_nop 5
	v_readlane_b32 s52, v3, 23
	v_cndmask_b32_e64 v6, 0, v3, s[18:19]
	s_nop 0
	v_rcp_f32_e64 v7, -s52
	v_writelane_b32 v36, s52, 7
	v_mul_f32_e32 v5, v6, v7
	s_nop 1
	v_mfma_f32_16x16x4_f32 v[0:3], v5, v3, v[0:3]
	v_mfma_f32_16x16x4_f32 a[4:7], v5, a7, a[4:7]
	s_nop 5
	v_readlane_b32 s52, v0, 40
	v_cndmask_b32_e64 v6, 0, v0, s[20:21]
	s_nop 0
	v_rcp_f32_e64 v7, -s52
	v_writelane_b32 v36, s52, 8
	v_mul_f32_e32 v4, v6, v7
	s_nop 1
	v_mfma_f32_16x16x4_f32 v[0:3], v4, v0, v[0:3]
	v_mfma_f32_16x16x4_f32 a[4:7], v4, a4, a[4:7]
	s_nop 5
	v_readlane_b32 s52, v1, 41
	v_cndmask_b32_e64 v6, 0, v1, s[22:23]
	s_nop 0
	v_rcp_f32_e64 v7, -s52
	v_writelane_b32 v36, s52, 9
	v_mul_f32_e32 v5, v6, v7
	s_nop 1
	v_mfma_f32_16x16x4_f32 v[0:3], v5, v1, v[0:3]
	v_mfma_f32_16x16x4_f32 a[4:7], v5, a5, a[4:7]
	s_nop 5
	v_readlane_b32 s52, v2, 42
	v_cndmask_b32_e64 v6, 0, v2, s[24:25]
	s_nop 0
	v_rcp_f32_e64 v7, -s52
	v_writelane_b32 v36, s52, 10
	v_mul_f32_e32 v4, v6, v7
	s_nop 1
	v_mfma_f32_16x16x4_f32 v[0:3], v4, v2, v[0:3]
	v_mfma_f32_16x16x4_f32 a[4:7], v4, a6, a[4:7]
	s_nop 5
	v_readlane_b32 s52, v3, 43
	v_cndmask_b32_e64 v6, 0, v3, s[26:27]
	s_nop 0
	v_rcp_f32_e64 v7, -s52
	v_writelane_b32 v36, s52, 11
	v_mul_f32_e32 v5, v6, v7
	s_nop 1
	v_mfma_f32_16x16x4_f32 v[0:3], v5, v3, v[0:3]
	v_mfma_f32_16x16x4_f32 a[4:7], v5, a7, a[4:7]
	s_nop 5
	v_readlane_b32 s52, v0, 60
	v_cndmask_b32_e64 v6, 0, v0, s[28:29]
	s_nop 0
	v_rcp_f32_e64 v7, -s52
	v_writelane_b32 v36, s52, 12
	v_mul_f32_e32 v4, v6, v7
	s_nop 1
	v_mfma_f32_16x16x4_f32 v[0:3], v4, v0, v[0:3]
	v_mfma_f32_16x16x4_f32 a[4:7], v4, a4, a[4:7]
	s_nop 5
	v_readlane_b32 s52, v1, 61
	v_cndmask_b32_e64 v6, 0, v1, s[30:31]
	s_nop 0
	v_rcp_f32_e64 v7, -s52
	v_writelane_b32 v36, s52, 13
	v_mul_f32_e32 v5, v6, v7
	s_nop 1
	v_mfma_f32_16x16x4_f32 v[0:3], v5, v1, v[0:3]
	v_mfma_f32_16x16x4_f32 a[4:7], v5, a5, a[4:7]
	s_nop 5
	v_readlane_b32 s52, v2, 62
	v_cndmask_b32_e64 v6, 0, v2, s[34:35]
	s_nop 0
	v_rcp_f32_e64 v7, -s52
	v_writelane_b32 v36, s52, 14
	v_mul_f32_e32 v4, v6, v7
	s_nop 1
	v_mfma_f32_16x16x4_f32 v[0:3], v4, v2, v[0:3]
	v_mfma_f32_16x16x4_f32 a[4:7], v4, a6, a[4:7]
	s_nop 5
	v_readlane_b32 s52, v3, 63
	s_nop 2
	v_writelane_b32 v36, s52, 15
	v_accvgpr_read_b32 v7, a7
	v_accvgpr_read_b32 v6, a6
	v_accvgpr_read_b32 v5, a5
	v_accvgpr_read_b32 v4, a4
	s_and_saveexec_b64 s[52:53], s[2:3]
	s_cbranch_execz .LBB1_345
	s_waitcnt lgkmcnt(2)
	v_lshl_add_u32 v37, s75, 2, v11
	ds_write_b32 v37, v36

.LBB1_355:
	s_add_i32 s81, s53, s80
	s_lshr_b32 vcc_lo, s81, 2
	s_add_i32 s81, s81, vcc_lo
	s_and_b32 s81, s81, 3
	s_cmp_lg_u32 s81, s86
	s_cbranch_scc1 .LBB1_354
	ds_read2_b32 v[4:5], v2 offset1:4
	v_add_u32_e32 v6, s79, v1
	v_add_u32_e32 v7, 0x1a900, v3
	ds_read2_b32 a[0:1], v6 offset1:68
	ds_read2_b32 a[2:3], v6 offset0:136 offset1:204
	ds_read_b32 v7, v7
	s_waitcnt lgkmcnt(3)
	v_xor_b32_e32 v4, 0x80000000, v4
	v_add_u32_e32 v14, 0x1a910, v3
	v_add_u32_e32 v34, 0x1a920, v3
	v_add_u32_e32 v35, 0x1a930, v3
	ds_read_b32 v14, v14
	ds_read_b32 v34, v34
	ds_read_b32 v35, v35
	s_waitcnt lgkmcnt(3)
	v_mfma_f32_16x16x4_f32 a[0:3], v4, v7, a[0:3]
	v_xor_b32_e32 v4, 0x80000000, v5
	s_waitcnt lgkmcnt(2)
	s_nop 0
	v_mfma_f32_16x16x4_f32 a[0:3], v4, v14, a[0:3]
	ds_read2_b32 v[4:5], v2 offset0:8 offset1:12
	s_waitcnt lgkmcnt(0)
	v_xor_b32_e32 v4, 0x80000000, v4
	s_nop 1
	v_mfma_f32_16x16x4_f32 a[0:3], v4, v34, a[0:3]
	v_xor_b32_e32 v4, 0x80000000, v5
	s_nop 1
	v_mfma_f32_16x16x4_f32 a[0:3], v4, v35, a[0:3]
	s_nop 9
	ds_write_b32 v6, a0
	ds_write_b32 v6, a1 offset:272
	ds_write_b32 v6, a2 offset:544
	ds_write_b32 v6, a3 offset:816
	s_branch .LBB1_354
